# MoBA gating loop: the eight block-mean LDS reads issued together before the FMAs (same FMA order)
# speedup vs baseline: 1.0019x; 1.0019x over previous
; #define LAS __attribute__((address_space(3)))
; __device__ __forceinline__ void moba_unit(Frame& F, const AttnBufs& A, int b, int h, int qb) {
;     ...
;     for (int j = 0; j < qb; ++j) {
;         float dot = 0.f;
; #pragma unroll
;         for (int d0 = 0; d0 < 4; ++d0) { const f32x4 ka = *(const LAS f32x4*)(KM + j * 64 + d0 * 16 + hi * 8), kb = *(const LAS f32x4*)(KM + j * 64 + d0 * 16 + hi * 8 + 4);
; #pragma unroll
;             for (int e = 0; e < 4; ++e) { dot += qf[8 * d0 + e] * ka[e]; dot += qf[8 * d0 + 4 + e] * kb[e]; } }
;         { auto rr = __builtin_amdgcn_permlane32_swap(__float_as_uint(dot), __float_as_uint(dot), false, false); dot = __uint_as_float(rr[0]) + __uint_as_float(rr[1]); }
;         if (dot > g0) { g2 = g1; i2 = i1; g1 = g0; i1 = i0; g0 = dot; i0 = j; } else if (dot > g1) { g2 = g1; i2 = i1; g1 = dot; i1 = j; } else if (dot > g2) { g2 = dot; i2 = j; }
;     }
.LBB0_285:
	v_add_u32_e32 v48, s23, v174
	v_add_u32_e32 v49, 0x18800, v48
	ds_read_b128 v[68:71], v49
	ds_read_b128 v[72:75], v49 offset:16
	ds_read_b128 v[52:55], v49 offset:64
	ds_read_b128 v[56:59], v49 offset:80
	ds_read_b128 v[60:63], v49 offset:128
	ds_read_b128 v[64:67], v49 offset:144
	ds_read_b128 v[40:43], v49 offset:192
	ds_read_b128 v[44:47], v49 offset:208
	s_waitcnt lgkmcnt(7)
	v_fma_f32 v50, v68, v18, 0
	s_waitcnt lgkmcnt(6)
	v_fmac_f32_e32 v50, v72, v20
	v_fmac_f32_e32 v50, v69, v14
	v_fmac_f32_e32 v50, v73, v16
	v_fmac_f32_e32 v50, v70, v19
	v_fmac_f32_e32 v50, v74, v21
	v_fmac_f32_e32 v50, v71, v15
	v_fmac_f32_e32 v50, v75, v17
	s_waitcnt lgkmcnt(5)
	v_fmac_f32_e32 v50, v52, v22
	s_waitcnt lgkmcnt(4)
	v_fmac_f32_e32 v50, v56, v26
	v_fmac_f32_e32 v50, v53, v23
	v_fmac_f32_e32 v50, v57, v12
	v_fmac_f32_e32 v50, v54, v24
	v_fmac_f32_e32 v50, v58, v27
	v_fmac_f32_e32 v50, v55, v25
	v_fmac_f32_e32 v50, v59, v13
	s_waitcnt lgkmcnt(3)
	v_fmac_f32_e32 v50, v60, v28
	s_waitcnt lgkmcnt(2)
	v_fmac_f32_e32 v50, v64, v32
	v_fmac_f32_e32 v50, v61, v29
	v_fmac_f32_e32 v50, v65, v33
	v_fmac_f32_e32 v50, v62, v30
	v_fmac_f32_e32 v50, v66, v34
	v_fmac_f32_e32 v50, v63, v31
	v_fmac_f32_e32 v50, v67, v35
	s_waitcnt lgkmcnt(1)
	v_mov_b32_e32 v49, v40
	s_waitcnt lgkmcnt(0)
	v_mov_b32_e32 v48, v44
	v_pk_mul_f32 v[48:49], v[48:49], v[6:7]
	s_nop 0
	v_add_f32_e32 v40, v49, v50
	v_add_f32_e32 v44, v48, v40
	v_mov_b32_e32 v40, v45
	v_pk_mul_f32 v[40:41], v[40:41], v[8:9]
	s_nop 0
	v_add_f32_e32 v41, v41, v44
	v_add_f32_e32 v44, v40, v41
	v_mov_b32_e32 v40, v46
	v_mov_b32_e32 v41, v42
	v_pk_mul_f32 v[40:41], v[40:41], v[10:11]
	v_mov_b32_e32 v42, v47
	v_add_f32_e32 v41, v41, v44
	v_add_f32_e32 v44, v40, v41
	v_pk_mul_f32 v[40:41], v[42:43], v[2:3]
	s_nop 0
	v_add_f32_e32 v41, v41, v44
	v_add_f32_e32 v40, v40, v41
	v_mov_b32_e32 v41, v40
	s_nop 1
	v_permlane32_swap_b32_e32 v40, v41
	v_add_f32_e32 v40, v40, v41
	v_cmp_ngt_f32_e32 vcc, v40, v37
	v_mov_b32_e32 v41, s26
	s_and_saveexec_b64 s[12:13], vcc
	s_cbranch_execz .LBB0_291
	v_cmp_ngt_f32_e32 vcc, v40, v36
	v_mov_b32_e32 v42, s26
	s_and_saveexec_b64 s[14:15], vcc
	s_cbranch_execz .LBB0_290
	v_cmp_gt_f32_e32 vcc, v40, v39
	s_and_saveexec_b64 s[16:17], vcc
	v_mov_b32_e32 v38, s26
	v_mov_b32_e32 v39, v40
	s_or_b64 exec, exec, s[16:17]
	v_mov_b32_e32 v42, v4
	v_mov_b32_e32 v40, v36
	v_mov_b32_e32 v36, v39
	v_mov_b32_e32 v4, v38
